# full stack + weight-conversion loop head waits vmcnt(4) (its 8 loads) instead of vmcnt(0) (which also waited for the previous item's 4 stores)
# speedup vs baseline: 1.0005x; 1.0005x over previous
.LBB0_218:
	v_add_u32_e32 v2, 0x800, v130
	s_lshr_b32 s0, s12, 8
	v_ashrrev_i32_e32 v41, 6, v2
	v_cvt_f32_u32_e32 v2, s0
	s_sub_i32 s13, 0, s0
	s_abs_i32 s9, s14
	s_ashr_i32 s8, s14, 31
	v_rcp_iflag_f32_e32 v2, v2
	v_add_u32_e32 v3, 0xa00, v130
	v_ashrrev_i32_e32 v42, 6, v3
	v_add_u32_e32 v3, 0xc00, v130
	v_mul_f32_e32 v2, 0x4f7ffffe, v2
	v_cvt_u32_f32_e32 v2, v2
	v_lshlrev_b32_e32 v1, 2, v130
	v_ashrrev_i32_e32 v43, 6, v3
	v_add_u32_e32 v3, 0xe00, v130
	v_readfirstlane_b32 s15, v2
	s_mul_i32 s13, s13, s15
	s_mul_hi_u32 s13, s15, s13
	s_add_i32 s15, s15, s13
	s_mul_hi_u32 s13, s9, s15
	s_mul_i32 s15, s13, s0
	s_sub_i32 s9, s9, s15
	s_add_i32 s15, s13, 1
	s_sub_i32 s16, s9, s0
	s_cmp_ge_u32 s9, s0
	s_cselect_b32 s13, s15, s13
	s_cselect_b32 s9, s16, s9
	s_add_i32 s15, s13, 1
	s_cmp_ge_u32 s9, s0
	s_cselect_b32 s9, s15, s13
	s_xor_b32 s9, s9, s8
	s_sub_i32 s13, s9, s8
	s_mul_i32 s0, s13, s0
	s_sub_i32 s0, s14, s0
	s_lshl_b32 s8, s0, 8
	s_ashr_i32 s9, s8, 31
	s_lshl_b64 s[14:15], s[8:9], 2
	s_add_u32 s10, s10, s14
	v_and_b32_e32 v36, 0xfc, v1
	v_ashrrev_i32_e32 v44, 6, v3
	s_addc_u32 s11, s11, s15
	s_lshl_b32 s16, s13, 6
	v_mov_b32_e32 v35, 0
	v_lshlrev_b32_e32 v34, 2, v36
	v_add_u32_e32 v4, s16, v44
	v_lshl_add_u64 v[2:3], s[10:11], 0, v[34:35]
	v_ashrrev_i32_e32 v7, 31, v4
	v_mad_u64_u32 v[4:5], s[10:11], v4, s12, 0
	v_mov_b32_e32 v6, v5
	v_mad_u64_u32 v[6:7], s[10:11], v7, s12, v[6:7]
	v_mov_b32_e32 v5, v6
	v_add_u32_e32 v6, s16, v43
	v_ashrrev_i32_e32 v9, 31, v6
	v_mad_u64_u32 v[6:7], s[10:11], v6, s12, 0
	v_mov_b32_e32 v8, v7
	v_mad_u64_u32 v[8:9], s[10:11], v9, s12, v[8:9]
	v_lshl_add_u64 v[4:5], v[4:5], 2, v[2:3]
	v_mov_b32_e32 v7, v8
	v_lshl_add_u64 v[6:7], v[6:7], 2, v[2:3]
	global_load_dwordx4 v[30:33], v[4:5], off
	global_load_dwordx4 v[26:29], v[6:7], off
	v_add_u32_e32 v4, s16, v42
	v_ashrrev_i32_e32 v7, 31, v4
	v_mad_u64_u32 v[4:5], s[10:11], v4, s12, 0
	v_mov_b32_e32 v6, v5
	v_mad_u64_u32 v[6:7], s[10:11], v7, s12, v[6:7]
	v_mov_b32_e32 v5, v6
	v_add_u32_e32 v6, s16, v41
	v_ashrrev_i32_e32 v9, 31, v6
	v_mad_u64_u32 v[6:7], s[10:11], v6, s12, 0
	v_mov_b32_e32 v8, v7
	v_add_u32_e32 v54, 0x600, v130
	v_mad_u64_u32 v[8:9], s[10:11], v9, s12, v[8:9]
	v_ashrrev_i32_e32 v40, 6, v54
	v_lshl_add_u64 v[4:5], v[4:5], 2, v[2:3]
	v_mov_b32_e32 v7, v8
	v_lshl_add_u64 v[6:7], v[6:7], 2, v[2:3]
	global_load_dwordx4 v[22:25], v[4:5], off
	global_load_dwordx4 v[18:21], v[6:7], off
	v_add_u32_e32 v4, s16, v40
	v_ashrrev_i32_e32 v7, 31, v4
	v_mad_u64_u32 v[4:5], s[10:11], v4, s12, 0
	v_add_u32_e32 v51, 0x400, v130
	v_mov_b32_e32 v6, v5
	v_ashrrev_i32_e32 v39, 6, v51
	v_mad_u64_u32 v[6:7], s[10:11], v7, s12, v[6:7]
	v_mov_b32_e32 v5, v6
	v_add_u32_e32 v6, s16, v39
	v_ashrrev_i32_e32 v9, 31, v6
	v_mad_u64_u32 v[6:7], s[10:11], v6, s12, 0
	v_mov_b32_e32 v8, v7
	v_add_u32_e32 v37, 0x200, v130
	v_mad_u64_u32 v[8:9], s[10:11], v9, s12, v[8:9]
	v_ashrrev_i32_e32 v38, 6, v37
	v_lshl_add_u64 v[4:5], v[4:5], 2, v[2:3]
	v_mov_b32_e32 v7, v8
	v_lshl_add_u64 v[6:7], v[6:7], 2, v[2:3]
	global_load_dwordx4 v[14:17], v[4:5], off
	global_load_dwordx4 v[10:13], v[6:7], off
	v_add_u32_e32 v4, s16, v38
	v_ashrrev_i32_e32 v7, 31, v4
	v_mad_u64_u32 v[4:5], s[10:11], v4, s12, 0
	v_mov_b32_e32 v6, v5
	v_ashrrev_i32_e32 v1, 6, v130
	v_mad_u64_u32 v[6:7], s[10:11], v7, s12, v[6:7]
	v_mov_b32_e32 v5, v6
	v_add_u32_e32 v6, s16, v1
	v_ashrrev_i32_e32 v9, 31, v6
	v_mad_u64_u32 v[6:7], s[10:11], v6, s12, 0
	v_mov_b32_e32 v8, v7
	v_mad_u64_u32 v[8:9], s[10:11], v9, s12, v[8:9]
	v_mov_b32_e32 v7, v8
	v_lshl_add_u64 v[4:5], v[4:5], 2, v[2:3]
	v_lshl_add_u64 v[2:3], v[6:7], 2, v[2:3]
	global_load_dwordx4 v[6:9], v[4:5], off
	s_nop 0
	global_load_dwordx4 v[2:5], v[2:3], off
	v_lshlrev_b32_e32 v45, 3, v130
	v_and_b32_e32 v66, 56, v45
	s_movk_i32 s0, 0x400
	v_mad_u32_u24 v55, v66, s0, 0
	v_mul_lo_u32 v57, v1, s0
	v_mul_lo_u32 v58, v38, s0
	v_mul_lo_u32 v59, v39, s0
	v_mul_lo_u32 v60, v40, s0
	v_mul_lo_u32 v61, v41, s0
	v_mul_lo_u32 v62, v42, s0
	v_mul_lo_u32 v63, v43, s0
	v_mul_lo_u32 v64, v44, s0
	s_add_u32 s0, s6, 0x1e940000
	s_addc_u32 s9, s7, 0
	s_add_u32 s12, s6, 0x16940000
	s_addc_u32 s13, s7, 0
	s_add_u32 s14, s6, 0x16140000
	s_addc_u32 s15, s7, 0
	s_add_u32 s30, s6, 0x15540000
	s_addc_u32 s31, s7, 0
	s_add_u32 s6, s6, 0x11f40000
	v_add_u32_e32 v34, 0, v34
	v_ashrrev_i32_e32 v45, 3, v130
	v_ashrrev_i32_e32 v48, 3, v37
	v_ashrrev_i32_e32 v51, 3, v51
	v_ashrrev_i32_e32 v54, 3, v54
	s_addc_u32 s7, s7, 0
	s_add_i32 s10, s33, s38
	s_mov_b32 s11, 0
	v_xor_b32_e32 v47, v45, v66
	v_lshl_add_u32 v46, v47, 2, v55
	v_and_b32_e32 v47, 15, v45
	v_xor_b32_e32 v50, v48, v66
	v_lshl_add_u32 v49, v50, 2, v55
	v_and_b32_e32 v50, 15, v48
	v_xor_b32_e32 v53, v51, v66
	v_lshl_add_u32 v52, v53, 2, v55
	v_and_b32_e32 v53, 15, v51
	v_xor_b32_e32 v56, v54, v66
	v_lshl_add_u32 v55, v56, 2, v55
	v_and_b32_e32 v56, 15, v54
	s_add_i32 s34, s10, 0xfffff5c0
	s_add_i32 s35, s10, 0xfffff6c0
	v_add_u32_e32 v57, v34, v57
	v_add_u32_e32 v58, v34, v58
	v_xor_b32_e32 v58, 32, v58
	v_add_u32_e32 v59, v34, v59
	v_xor_b32_e32 v59, 64, v59
	v_add_u32_e32 v60, v34, v60
	v_xor_b32_e32 v60, 96, v60
	v_add_u32_e32 v61, v34, v61
	v_xor_b32_e32 v61, 128, v61
	v_add_u32_e32 v62, v34, v62
	v_xor_b32_e32 v62, 160, v62
	v_add_u32_e32 v63, v34, v63
	v_xor_b32_e32 v63, 192, v63
	v_add_u32_e32 v64, v34, v64
	v_xor_b32_e32 v64, 224, v64
	v_lshlrev_b32_e32 v34, 2, v36
	v_lshlrev_b32_e32 v36, 1, v66
	s_movk_i32 s36, 0x7fff
	v_mov_b32_e32 v65, 1
	s_mov_b32 s26, s17
	s_mov_b32 s27, s29
	s_mov_b64 s[20:21], s[2:3]
	s_waitcnt vmcnt(0)
	s_branch .LBB0_222

.LBB0_222:
	s_add_i32 s33, s33, s38
	s_cmp_lt_u32 s28, 2
	s_cselect_b64 s[18:19], -1, 0
	s_and_b64 vcc, exec, s[18:19]
	s_mov_b32 s37, s1
	s_mov_b32 s22, s8
	s_mov_b32 s10, s16
	s_waitcnt vmcnt(4)
	ds_write_b128 v57, v[2:5]
	ds_write_b128 v58, v[6:9]
	ds_write_b128 v59, v[10:13]
	ds_write_b128 v60, v[14:17]
	ds_write_b128 v61, v[18:21]
	ds_write_b128 v62, v[22:25]
	ds_write_b128 v63, v[26:29]
	ds_write_b128 v64, v[30:33]
	s_waitcnt lgkmcnt(0)
	s_barrier
	s_cbranch_vccnz .LBB0_221
	s_add_i32 s10, s34, 0xa40
	s_cmpk_lt_i32 s10, 0x6c0
	s_cbranch_scc1 .LBB0_219
	s_cmpk_gt_u32 s10, 0x83f
	s_mov_b64 s[22:23], -1
	s_cbranch_scc0 .LBB0_237
	s_cmpk_gt_u32 s10, 0x93f
	s_cbranch_scc0 .LBB0_234
	s_mul_hi_u32 s10, s35, 0xaaaaaaab
	s_lshr_b32 s10, s10, 8
	s_mul_i32 s20, s10, 0xfffffe80
	s_add_i32 s10, s34, 0x100
	s_mul_hi_u32 s10, s10, 0xaaaaaaab
	s_lshr_b32 s10, s10, 8
	s_mul_i32 s21, s10, 0xfffffe80
	s_add_i32 s41, s33, s21
	s_add_i32 s40, s34, s20
	s_addk_i32 s41, 0xf6c0
	s_add_i32 s42, s40, 0x100
	s_cmpk_gt_i32 s42, 0x7f
	s_cbranch_scc0 .LBB0_231
	s_lshl_b64 s[22:23], s[10:11], 23
	s_cmpk_gt_u32 s42, 0xff
	s_mov_b64 s[26:27], -1
	s_cbranch_scc0 .LBB0_229
	s_add_u32 s24, s88, s22
	s_addc_u32 s25, s89, s23
	s_lshl_b64 s[20:21], s[10:11], 22
	s_add_u32 s20, s0, s20
	s_addc_u32 s21, s9, s21
	s_mov_b64 s[26:27], 0

.LBB0_1942:
	s_waitcnt vmcnt(11)
	v_add_u32_e32 v2, 0x800, v34
	s_lshr_b32 s4, s8, 8
	v_ashrrev_i32_e32 v42, 6, v2
	v_cvt_f32_u32_e32 v2, s4
	s_sub_i32 s11, 0, s4
	s_abs_i32 s10, s9
	s_ashr_i32 s5, s9, 31
	v_rcp_iflag_f32_e32 v2, v2
	v_add_u32_e32 v3, 0xa00, v34
	v_ashrrev_i32_e32 v43, 6, v3
	v_add_u32_e32 v3, 0xc00, v34
	v_mul_f32_e32 v2, 0x4f7ffffe, v2
	v_cvt_u32_f32_e32 v2, v2
	v_lshlrev_b32_e32 v1, 2, v34
	v_ashrrev_i32_e32 v44, 6, v3
	v_add_u32_e32 v3, 0xe00, v34
	v_readfirstlane_b32 s12, v2
	s_mul_i32 s11, s11, s12
	s_mul_hi_u32 s11, s12, s11
	s_add_i32 s12, s12, s11
	s_mul_hi_u32 s11, s10, s12
	s_mul_i32 s12, s11, s4
	s_sub_i32 s10, s10, s12
	s_add_i32 s12, s11, 1
	s_sub_i32 s13, s10, s4
	s_cmp_ge_u32 s10, s4
	s_cselect_b32 s11, s12, s11
	s_cselect_b32 s10, s13, s10
	s_add_i32 s12, s11, 1
	s_cmp_ge_u32 s10, s4
	s_cselect_b32 s10, s12, s11
	s_xor_b32 s10, s10, s5
	s_sub_i32 s12, s10, s5
	s_mul_i32 s4, s12, s4
	s_sub_i32 s4, s9, s4
	s_lshl_b32 s4, s4, 8
	s_ashr_i32 s5, s4, 31
	s_lshl_b64 s[10:11], s[4:5], 2
	s_add_u32 s6, s6, s10
	v_and_b32_e32 v38, 0xfc, v1
	v_ashrrev_i32_e32 v45, 6, v3
	s_addc_u32 s7, s7, s11
	s_lshl_b32 s14, s12, 6
	v_mov_b32_e32 v37, 0
	v_lshlrev_b32_e32 v36, 2, v38
	v_add_u32_e32 v4, s14, v45
	v_lshl_add_u64 v[2:3], s[6:7], 0, v[36:37]
	s_waitcnt vmcnt(10)
	v_ashrrev_i32_e32 v7, 31, v4
	v_mad_u64_u32 v[4:5], s[6:7], v4, s8, 0
	v_mov_b32_e32 v6, v5
	v_mad_u64_u32 v[6:7], s[6:7], v7, s8, v[6:7]
	v_mov_b32_e32 v5, v6
	v_add_u32_e32 v6, s14, v44
	v_ashrrev_i32_e32 v9, 31, v6
	v_mad_u64_u32 v[6:7], s[6:7], v6, s8, 0
	v_mov_b32_e32 v8, v7
	v_mad_u64_u32 v[8:9], s[6:7], v9, s8, v[8:9]
	v_lshl_add_u64 v[4:5], v[4:5], 2, v[2:3]
	v_mov_b32_e32 v7, v8
	v_lshl_add_u64 v[6:7], v[6:7], 2, v[2:3]
	global_load_dwordx4 v[30:33], v[4:5], off
	global_load_dwordx4 v[26:29], v[6:7], off
	v_add_u32_e32 v4, s14, v43
	v_ashrrev_i32_e32 v7, 31, v4
	v_mad_u64_u32 v[4:5], s[6:7], v4, s8, 0
	v_mov_b32_e32 v6, v5
	v_mad_u64_u32 v[6:7], s[6:7], v7, s8, v[6:7]
	v_mov_b32_e32 v5, v6
	v_add_u32_e32 v6, s14, v42
	v_ashrrev_i32_e32 v9, 31, v6
	v_mad_u64_u32 v[6:7], s[6:7], v6, s8, 0
	v_mov_b32_e32 v8, v7
	v_add_u32_e32 v55, 0x600, v34
	v_mad_u64_u32 v[8:9], s[6:7], v9, s8, v[8:9]
	v_ashrrev_i32_e32 v41, 6, v55
	v_lshl_add_u64 v[4:5], v[4:5], 2, v[2:3]
	v_mov_b32_e32 v7, v8
	v_lshl_add_u64 v[6:7], v[6:7], 2, v[2:3]
	global_load_dwordx4 v[22:25], v[4:5], off
	global_load_dwordx4 v[18:21], v[6:7], off
	v_add_u32_e32 v4, s14, v41
	v_ashrrev_i32_e32 v7, 31, v4
	v_mad_u64_u32 v[4:5], s[6:7], v4, s8, 0
	v_add_u32_e32 v52, 0x400, v34
	v_mov_b32_e32 v6, v5
	v_ashrrev_i32_e32 v40, 6, v52
	v_mad_u64_u32 v[6:7], s[6:7], v7, s8, v[6:7]
	v_mov_b32_e32 v5, v6
	v_add_u32_e32 v6, s14, v40
	v_ashrrev_i32_e32 v9, 31, v6
	v_mad_u64_u32 v[6:7], s[6:7], v6, s8, 0
	v_mov_b32_e32 v8, v7
	v_add_u32_e32 v39, 0x200, v34
	v_mad_u64_u32 v[8:9], s[6:7], v9, s8, v[8:9]
	v_ashrrev_i32_e32 v35, 6, v39
	v_lshl_add_u64 v[4:5], v[4:5], 2, v[2:3]
	v_mov_b32_e32 v7, v8
	v_lshl_add_u64 v[6:7], v[6:7], 2, v[2:3]
	global_load_dwordx4 v[14:17], v[4:5], off
	global_load_dwordx4 v[10:13], v[6:7], off
	v_add_u32_e32 v4, s14, v35
	v_ashrrev_i32_e32 v7, 31, v4
	v_mad_u64_u32 v[4:5], s[6:7], v4, s8, 0
	v_mov_b32_e32 v6, v5
	v_ashrrev_i32_e32 v1, 6, v34
	v_mad_u64_u32 v[6:7], s[6:7], v7, s8, v[6:7]
	v_mov_b32_e32 v5, v6
	v_add_u32_e32 v6, s14, v1
	v_ashrrev_i32_e32 v9, 31, v6
	v_mad_u64_u32 v[6:7], s[6:7], v6, s8, 0
	v_mov_b32_e32 v8, v7
	v_mad_u64_u32 v[8:9], s[6:7], v9, s8, v[8:9]
	v_mov_b32_e32 v7, v8
	v_lshl_add_u64 v[4:5], v[4:5], 2, v[2:3]
	v_lshl_add_u64 v[2:3], v[6:7], 2, v[2:3]
	global_load_dwordx4 v[6:9], v[4:5], off
	s_nop 0
	global_load_dwordx4 v[2:5], v[2:3], off
	v_lshlrev_b32_e32 v46, 3, v34
	v_and_b32_e32 v66, 56, v46
	s_movk_i32 s5, 0x400
	v_readlane_b32 s12, v251, 60
	v_mad_u32_u24 v56, v66, s5, 0
	v_mul_lo_u32 v58, v1, s5
	v_mul_lo_u32 v59, v35, s5
	v_mul_lo_u32 v60, v40, s5
	v_mul_lo_u32 v61, v41, s5
	v_mul_lo_u32 v62, v42, s5
	v_mul_lo_u32 v63, v43, s5
	v_mul_lo_u32 v64, v44, s5
	v_mul_lo_u32 v65, v45, s5
	v_readlane_b32 s13, v251, 61
	s_add_u32 s5, s12, 0x1e940000
	s_addc_u32 s26, s13, 0
	s_add_u32 s8, s12, 0x16940000
	s_addc_u32 s9, s13, 0
	s_add_u32 s10, s12, 0x16140000
	s_addc_u32 s11, s13, 0
	s_add_u32 s27, s12, 0x15540000
	s_addc_u32 s28, s13, 0
	v_add_u32_e32 v36, 0, v36
	v_ashrrev_i32_e32 v46, 3, v34
	v_ashrrev_i32_e32 v49, 3, v39
	v_ashrrev_i32_e32 v52, 3, v52
	v_ashrrev_i32_e32 v55, 3, v55
	s_add_u32 s12, s12, 0x11f40000
	s_mov_b32 s7, 0
	v_xor_b32_e32 v48, v46, v66
	v_lshl_add_u32 v47, v48, 2, v56
	v_and_b32_e32 v48, 15, v46
	v_xor_b32_e32 v51, v49, v66
	v_lshl_add_u32 v50, v51, 2, v56
	v_and_b32_e32 v51, 15, v49
	v_xor_b32_e32 v54, v52, v66
	v_lshl_add_u32 v53, v54, 2, v56
	v_and_b32_e32 v54, 15, v52
	v_xor_b32_e32 v57, v55, v66
	v_lshl_add_u32 v56, v57, 2, v56
	v_and_b32_e32 v57, 15, v55
	s_addc_u32 s13, s13, 0
	s_add_i32 s29, s16, 0x15e1
	s_mov_b32 s30, 17
	v_add_u32_e32 v58, v36, v58
	v_add_u32_e32 v59, v36, v59
	v_xor_b32_e32 v59, 32, v59
	v_add_u32_e32 v60, v36, v60
	v_xor_b32_e32 v60, 64, v60
	v_add_u32_e32 v61, v36, v61
	v_xor_b32_e32 v61, 96, v61
	v_add_u32_e32 v62, v36, v62
	v_xor_b32_e32 v62, 128, v62
	v_add_u32_e32 v63, v36, v63
	v_xor_b32_e32 v63, 160, v63
	v_add_u32_e32 v64, v36, v64
	v_xor_b32_e32 v64, 192, v64
	v_add_u32_e32 v65, v36, v65
	v_xor_b32_e32 v65, 224, v65
	v_lshlrev_b32_e32 v36, 2, v38
	v_lshlrev_b32_e32 v38, 1, v66
	s_movk_i32 s31, 0x7fff
	v_mov_b32_e32 v66, 1
	s_mov_b32 s24, s15
	s_mov_b32 s25, s0
	s_mov_b64 s[18:19], s[2:3]
	v_readlane_b32 s42, v251, 58
	v_readlane_b32 s43, v251, 59
	s_waitcnt vmcnt(0)
	s_branch .LBB0_1946

.LBB0_1946:
	s_add_i32 s33, s34, 1
	s_cmp_lt_u32 s30, 2
	s_cselect_b64 s[16:17], -1, 0
	s_and_b64 vcc, exec, s[16:17]
	s_mov_b32 s35, s1
	s_mov_b32 s20, s4
	s_mov_b32 s6, s14
	s_waitcnt vmcnt(4)
	ds_write_b128 v58, v[2:5]
	ds_write_b128 v59, v[6:9]
	ds_write_b128 v60, v[10:13]
	ds_write_b128 v61, v[14:17]
	ds_write_b128 v62, v[18:21]
	ds_write_b128 v63, v[22:25]
	ds_write_b128 v64, v[26:29]
	ds_write_b128 v65, v[30:33]
	s_waitcnt lgkmcnt(0)
	s_barrier
	s_cbranch_vccnz .LBB0_1945
	s_add_i32 s6, s29, 0x93f
	s_cmpk_lt_i32 s6, 0x6bf
	s_cbranch_scc1 .LBB0_1943
	s_add_i32 s6, s29, 0x940
	s_cmpk_gt_u32 s6, 0x83f
	s_mov_b64 s[20:21], -1
	s_cbranch_scc0 .LBB0_1961
	s_cmpk_gt_u32 s6, 0x93f
	s_cbranch_scc0 .LBB0_1958
	s_mul_hi_u32 s6, s29, 0xaaaaaaab
	s_lshr_b32 s6, s6, 8
	s_mul_i32 s18, s6, 0xfffffe80
	s_add_i32 s34, s34, s18
	s_addk_i32 s34, 0xf6c1
	s_add_i32 s38, s29, s18
	s_cmpk_gt_i32 s38, 0x7f
	s_cbranch_scc0 .LBB0_1955
	s_lshl_b64 s[20:21], s[6:7], 23
	s_cmpk_gt_u32 s38, 0xff
	s_mov_b64 s[24:25], -1
	s_cbranch_scc0 .LBB0_1953
	s_add_i32 s37, s34, 0xffffff00
	s_add_u32 s22, s88, s20
	s_addc_u32 s23, s89, s21
	s_lshl_b64 s[18:19], s[6:7], 22
	s_add_u32 s18, s5, s18
	s_addc_u32 s19, s26, s19
	s_mov_b64 s[24:25], 0

.LBB0_1991:
	s_waitcnt vmcnt(11)
	v_add_u32_e32 v2, 0x800, v34
	s_lshr_b32 s0, s8, 8
	v_ashrrev_i32_e32 v42, 6, v2
	v_cvt_f32_u32_e32 v2, s0
	s_sub_i32 s9, 0, s0
	s_abs_i32 s5, s10
	s_ashr_i32 s4, s10, 31
	v_rcp_iflag_f32_e32 v2, v2
	v_add_u32_e32 v3, 0xa00, v34
	v_ashrrev_i32_e32 v43, 6, v3
	v_add_u32_e32 v3, 0xc00, v34
	v_mul_f32_e32 v2, 0x4f7ffffe, v2
	v_cvt_u32_f32_e32 v2, v2
	v_lshlrev_b32_e32 v1, 2, v34
	v_ashrrev_i32_e32 v44, 6, v3
	v_add_u32_e32 v3, 0xe00, v34
	v_readfirstlane_b32 s11, v2
	s_mul_i32 s9, s9, s11
	s_mul_hi_u32 s9, s11, s9
	s_add_i32 s11, s11, s9
	s_mul_hi_u32 s9, s5, s11
	s_mul_i32 s11, s9, s0
	s_sub_i32 s5, s5, s11
	s_add_i32 s11, s9, 1
	s_sub_i32 s12, s5, s0
	s_cmp_ge_u32 s5, s0
	s_cselect_b32 s9, s11, s9
	s_cselect_b32 s5, s12, s5
	s_add_i32 s11, s9, 1
	s_cmp_ge_u32 s5, s0
	s_cselect_b32 s5, s11, s9
	s_xor_b32 s5, s5, s4
	s_sub_i32 s9, s5, s4
	s_mul_i32 s0, s9, s0
	s_sub_i32 s0, s10, s0
	s_lshl_b32 s4, s0, 8
	s_ashr_i32 s5, s4, 31
	s_lshl_b64 s[10:11], s[4:5], 2
	s_add_u32 s6, s6, s10
	v_and_b32_e32 v38, 0xfc, v1
	v_ashrrev_i32_e32 v45, 6, v3
	s_addc_u32 s7, s7, s11
	s_lshl_b32 s14, s9, 6
	v_mov_b32_e32 v37, 0
	v_lshlrev_b32_e32 v36, 2, v38
	v_add_u32_e32 v4, s14, v45
	v_lshl_add_u64 v[2:3], s[6:7], 0, v[36:37]
	s_waitcnt vmcnt(10)
	v_ashrrev_i32_e32 v7, 31, v4
	v_mad_u64_u32 v[4:5], s[6:7], v4, s8, 0
	v_mov_b32_e32 v6, v5
	v_mad_u64_u32 v[6:7], s[6:7], v7, s8, v[6:7]
	v_mov_b32_e32 v5, v6
	v_add_u32_e32 v6, s14, v44
	v_ashrrev_i32_e32 v9, 31, v6
	v_mad_u64_u32 v[6:7], s[6:7], v6, s8, 0
	v_mov_b32_e32 v8, v7
	v_mad_u64_u32 v[8:9], s[6:7], v9, s8, v[8:9]
	v_lshl_add_u64 v[4:5], v[4:5], 2, v[2:3]
	v_mov_b32_e32 v7, v8
	v_lshl_add_u64 v[6:7], v[6:7], 2, v[2:3]
	global_load_dwordx4 v[30:33], v[4:5], off
	global_load_dwordx4 v[26:29], v[6:7], off
	v_add_u32_e32 v4, s14, v43
	v_ashrrev_i32_e32 v7, 31, v4
	v_mad_u64_u32 v[4:5], s[6:7], v4, s8, 0
	v_mov_b32_e32 v6, v5
	v_mad_u64_u32 v[6:7], s[6:7], v7, s8, v[6:7]
	v_mov_b32_e32 v5, v6
	v_add_u32_e32 v6, s14, v42
	v_ashrrev_i32_e32 v9, 31, v6
	v_mad_u64_u32 v[6:7], s[6:7], v6, s8, 0
	v_mov_b32_e32 v8, v7
	v_add_u32_e32 v55, 0x600, v34
	v_mad_u64_u32 v[8:9], s[6:7], v9, s8, v[8:9]
	v_ashrrev_i32_e32 v41, 6, v55
	v_lshl_add_u64 v[4:5], v[4:5], 2, v[2:3]
	v_mov_b32_e32 v7, v8
	v_lshl_add_u64 v[6:7], v[6:7], 2, v[2:3]
	global_load_dwordx4 v[22:25], v[4:5], off
	global_load_dwordx4 v[18:21], v[6:7], off
	v_add_u32_e32 v4, s14, v41
	v_ashrrev_i32_e32 v7, 31, v4
	v_mad_u64_u32 v[4:5], s[6:7], v4, s8, 0
	v_add_u32_e32 v52, 0x400, v34
	v_mov_b32_e32 v6, v5
	v_ashrrev_i32_e32 v40, 6, v52
	v_mad_u64_u32 v[6:7], s[6:7], v7, s8, v[6:7]
	v_mov_b32_e32 v5, v6
	v_add_u32_e32 v6, s14, v40
	v_ashrrev_i32_e32 v9, 31, v6
	v_mad_u64_u32 v[6:7], s[6:7], v6, s8, 0
	v_mov_b32_e32 v8, v7
	v_add_u32_e32 v35, 0x200, v34
	v_mad_u64_u32 v[8:9], s[6:7], v9, s8, v[8:9]
	v_ashrrev_i32_e32 v39, 6, v35
	v_lshl_add_u64 v[4:5], v[4:5], 2, v[2:3]
	v_mov_b32_e32 v7, v8
	v_lshl_add_u64 v[6:7], v[6:7], 2, v[2:3]
	global_load_dwordx4 v[14:17], v[4:5], off
	global_load_dwordx4 v[10:13], v[6:7], off
	v_add_u32_e32 v4, s14, v39
	v_ashrrev_i32_e32 v7, 31, v4
	v_mad_u64_u32 v[4:5], s[6:7], v4, s8, 0
	v_mov_b32_e32 v6, v5
	v_ashrrev_i32_e32 v1, 6, v34
	v_mad_u64_u32 v[6:7], s[6:7], v7, s8, v[6:7]
	v_mov_b32_e32 v5, v6
	v_add_u32_e32 v6, s14, v1
	v_ashrrev_i32_e32 v9, 31, v6
	v_mad_u64_u32 v[6:7], s[6:7], v6, s8, 0
	v_mov_b32_e32 v8, v7
	v_mad_u64_u32 v[8:9], s[6:7], v9, s8, v[8:9]
	v_mov_b32_e32 v7, v8
	v_lshl_add_u64 v[4:5], v[4:5], 2, v[2:3]
	v_lshl_add_u64 v[2:3], v[6:7], 2, v[2:3]
	global_load_dwordx4 v[6:9], v[4:5], off
	s_nop 0
	global_load_dwordx4 v[2:5], v[2:3], off
	v_lshlrev_b32_e32 v46, 3, v34
	v_and_b32_e32 v66, 56, v46
	s_movk_i32 s0, 0x400
	v_readlane_b32 s12, v251, 60
	v_mad_u32_u24 v56, v66, s0, 0
	v_mul_lo_u32 v58, v1, s0
	v_mul_lo_u32 v59, v39, s0
	v_mul_lo_u32 v60, v40, s0
	v_mul_lo_u32 v61, v41, s0
	v_mul_lo_u32 v62, v42, s0
	v_mul_lo_u32 v63, v43, s0
	v_mul_lo_u32 v64, v44, s0
	v_mul_lo_u32 v65, v45, s0
	v_readlane_b32 s13, v251, 61
	s_add_u32 s0, s12, 0x1e940000
	s_addc_u32 s5, s13, 0
	s_add_u32 s8, s12, 0x16940000
	s_addc_u32 s9, s13, 0
	s_add_u32 s10, s12, 0x16140000
	s_addc_u32 s11, s13, 0
	s_add_u32 s27, s12, 0x15540000
	s_addc_u32 s28, s13, 0
	v_add_u32_e32 v36, 0, v36
	v_ashrrev_i32_e32 v46, 3, v34
	v_ashrrev_i32_e32 v49, 3, v35
	v_ashrrev_i32_e32 v52, 3, v52
	v_ashrrev_i32_e32 v55, 3, v55
	s_add_u32 s12, s12, 0x11f40000
	s_mov_b32 s7, 0
	v_xor_b32_e32 v48, v46, v66
	v_lshl_add_u32 v47, v48, 2, v56
	v_and_b32_e32 v48, 15, v46
	v_xor_b32_e32 v51, v49, v66
	v_lshl_add_u32 v50, v51, 2, v56
	v_and_b32_e32 v51, 15, v49
	v_xor_b32_e32 v54, v52, v66
	v_lshl_add_u32 v53, v54, 2, v56
	v_and_b32_e32 v54, 15, v52
	v_xor_b32_e32 v57, v55, v66
	v_lshl_add_u32 v56, v57, 2, v56
	v_and_b32_e32 v57, 15, v55
	s_addc_u32 s13, s13, 0
	s_add_i32 s29, s16, 0xfffffce1
	s_mov_b32 s30, 25
	v_add_u32_e32 v58, v36, v58
	v_add_u32_e32 v59, v36, v59
	v_xor_b32_e32 v59, 32, v59
	v_add_u32_e32 v60, v36, v60
	v_xor_b32_e32 v60, 64, v60
	v_add_u32_e32 v61, v36, v61
	v_xor_b32_e32 v61, 96, v61
	v_add_u32_e32 v62, v36, v62
	v_xor_b32_e32 v62, 128, v62
	v_add_u32_e32 v63, v36, v63
	v_xor_b32_e32 v63, 160, v63
	v_add_u32_e32 v64, v36, v64
	v_xor_b32_e32 v64, 192, v64
	v_add_u32_e32 v65, v36, v65
	v_xor_b32_e32 v65, 224, v65
	v_lshlrev_b32_e32 v36, 2, v38
	v_lshlrev_b32_e32 v34, 1, v66
	s_movk_i32 s31, 0x7fff
	v_mov_b32_e32 v38, 1
	s_mov_b32 s24, s15
	s_mov_b32 s25, s26
	s_mov_b64 s[18:19], s[2:3]
	s_waitcnt vmcnt(0)
	s_branch .LBB0_1995

.LBB0_1995:
	s_add_i32 s33, s34, 1
	s_cmp_lt_u32 s30, 2
	s_cselect_b64 s[16:17], -1, 0
	s_and_b64 vcc, exec, s[16:17]
	s_mov_b32 s35, s1
	s_mov_b32 s20, s4
	s_mov_b32 s6, s14
	s_waitcnt vmcnt(4)
	ds_write_b128 v58, v[2:5]
	ds_write_b128 v59, v[6:9]
	ds_write_b128 v60, v[10:13]
	ds_write_b128 v61, v[14:17]
	ds_write_b128 v62, v[18:21]
	ds_write_b128 v63, v[22:25]
	ds_write_b128 v64, v[26:29]
	ds_write_b128 v65, v[30:33]
	s_waitcnt lgkmcnt(0)
	s_barrier
	s_cbranch_vccnz .LBB0_1994
	s_add_i32 s6, s29, 0x93f
	s_cmpk_lt_i32 s6, 0x6bf
	s_cbranch_scc1 .LBB0_1992
	s_add_i32 s6, s29, 0x940
	s_cmpk_gt_u32 s6, 0x83f
	s_mov_b64 s[20:21], -1
	s_cbranch_scc0 .LBB0_2010
	s_cmpk_gt_u32 s6, 0x93f
	s_cbranch_scc0 .LBB0_2007
	s_mul_hi_u32 s6, s29, 0xaaaaaaab
	s_lshr_b32 s6, s6, 8
	s_mul_i32 s18, s6, 0xfffffe80
	s_add_i32 s34, s34, s18
	s_addk_i32 s34, 0xf6c1
	s_add_i32 s38, s29, s18
	s_cmpk_gt_i32 s38, 0x7f
	s_cbranch_scc0 .LBB0_2004
	s_lshl_b64 s[20:21], s[6:7], 23
	s_cmpk_gt_u32 s38, 0xff
	s_mov_b64 s[24:25], -1
	s_cbranch_scc0 .LBB0_2002
	s_add_i32 s37, s34, 0xffffff00
	s_add_u32 s22, s88, s20
	s_addc_u32 s23, s89, s21
	s_lshl_b64 s[18:19], s[6:7], 22
	s_add_u32 s18, s0, s18
	s_addc_u32 s19, s5, s19
	s_mov_b64 s[24:25], 0

.LBB0_2313:
	s_waitcnt vmcnt(11)
	v_add_u32_e32 v2, 0x800, v130
	s_lshr_b32 s0, s12, 8
	v_ashrrev_i32_e32 v41, 6, v2
	v_cvt_f32_u32_e32 v2, s0
	s_sub_i32 s14, 0, s0
	s_abs_i32 s9, s13
	s_ashr_i32 s8, s13, 31
	v_rcp_iflag_f32_e32 v2, v2
	v_add_u32_e32 v3, 0xa00, v130
	v_ashrrev_i32_e32 v42, 6, v3
	v_add_u32_e32 v3, 0xc00, v130
	v_mul_f32_e32 v2, 0x4f7ffffe, v2
	v_cvt_u32_f32_e32 v2, v2
	v_lshlrev_b32_e32 v1, 2, v130
	v_ashrrev_i32_e32 v43, 6, v3
	v_add_u32_e32 v3, 0xe00, v130
	v_readfirstlane_b32 s15, v2
	s_mul_i32 s14, s14, s15
	s_mul_hi_u32 s14, s15, s14
	s_add_i32 s15, s15, s14
	s_mul_hi_u32 s14, s9, s15
	s_mul_i32 s15, s14, s0
	s_sub_i32 s9, s9, s15
	s_add_i32 s15, s14, 1
	s_sub_i32 s16, s9, s0
	s_cmp_ge_u32 s9, s0
	s_cselect_b32 s14, s15, s14
	s_cselect_b32 s9, s16, s9
	s_add_i32 s15, s14, 1
	s_cmp_ge_u32 s9, s0
	s_cselect_b32 s9, s15, s14
	s_xor_b32 s9, s9, s8
	s_sub_i32 s16, s9, s8
	s_mul_i32 s0, s16, s0
	s_sub_i32 s0, s13, s0
	s_lshl_b32 s8, s0, 8
	s_ashr_i32 s9, s8, 31
	s_lshl_b64 s[14:15], s[8:9], 2
	s_add_u32 s10, s10, s14
	v_and_b32_e32 v36, 0xfc, v1
	v_ashrrev_i32_e32 v44, 6, v3
	s_addc_u32 s11, s11, s15
	s_lshl_b32 s20, s16, 6
	v_mov_b32_e32 v35, 0
	v_lshlrev_b32_e32 v34, 2, v36
	v_add_u32_e32 v4, s20, v44
	v_lshl_add_u64 v[2:3], s[10:11], 0, v[34:35]
	s_waitcnt vmcnt(10)
	v_ashrrev_i32_e32 v7, 31, v4
	v_mad_u64_u32 v[4:5], s[10:11], v4, s12, 0
	v_mov_b32_e32 v6, v5
	v_mad_u64_u32 v[6:7], s[10:11], v7, s12, v[6:7]
	v_mov_b32_e32 v5, v6
	v_add_u32_e32 v6, s20, v43
	v_ashrrev_i32_e32 v9, 31, v6
	v_mad_u64_u32 v[6:7], s[10:11], v6, s12, 0
	v_mov_b32_e32 v8, v7
	v_mad_u64_u32 v[8:9], s[10:11], v9, s12, v[8:9]
	v_lshl_add_u64 v[4:5], v[4:5], 2, v[2:3]
	v_mov_b32_e32 v7, v8
	v_lshl_add_u64 v[6:7], v[6:7], 2, v[2:3]
	global_load_dwordx4 v[30:33], v[4:5], off
	global_load_dwordx4 v[26:29], v[6:7], off
	v_add_u32_e32 v4, s20, v42
	v_ashrrev_i32_e32 v7, 31, v4
	v_mad_u64_u32 v[4:5], s[10:11], v4, s12, 0
	v_mov_b32_e32 v6, v5
	v_mad_u64_u32 v[6:7], s[10:11], v7, s12, v[6:7]
	v_mov_b32_e32 v5, v6
	v_add_u32_e32 v6, s20, v41
	v_ashrrev_i32_e32 v9, 31, v6
	v_mad_u64_u32 v[6:7], s[10:11], v6, s12, 0
	v_mov_b32_e32 v8, v7
	v_add_u32_e32 v54, 0x600, v130
	v_mad_u64_u32 v[8:9], s[10:11], v9, s12, v[8:9]
	v_ashrrev_i32_e32 v40, 6, v54
	v_lshl_add_u64 v[4:5], v[4:5], 2, v[2:3]
	v_mov_b32_e32 v7, v8
	v_lshl_add_u64 v[6:7], v[6:7], 2, v[2:3]
	global_load_dwordx4 v[22:25], v[4:5], off
	global_load_dwordx4 v[18:21], v[6:7], off
	v_add_u32_e32 v4, s20, v40
	v_ashrrev_i32_e32 v7, 31, v4
	v_mad_u64_u32 v[4:5], s[10:11], v4, s12, 0
	v_add_u32_e32 v51, 0x400, v130
	v_mov_b32_e32 v6, v5
	v_ashrrev_i32_e32 v39, 6, v51
	v_mad_u64_u32 v[6:7], s[10:11], v7, s12, v[6:7]
	v_mov_b32_e32 v5, v6
	v_add_u32_e32 v6, s20, v39
	v_ashrrev_i32_e32 v9, 31, v6
	v_mad_u64_u32 v[6:7], s[10:11], v6, s12, 0
	v_mov_b32_e32 v8, v7
	v_add_u32_e32 v37, 0x200, v130
	v_mad_u64_u32 v[8:9], s[10:11], v9, s12, v[8:9]
	v_ashrrev_i32_e32 v38, 6, v37
	v_lshl_add_u64 v[4:5], v[4:5], 2, v[2:3]
	v_mov_b32_e32 v7, v8
	v_lshl_add_u64 v[6:7], v[6:7], 2, v[2:3]
	global_load_dwordx4 v[14:17], v[4:5], off
	global_load_dwordx4 v[10:13], v[6:7], off
	v_add_u32_e32 v4, s20, v38
	v_ashrrev_i32_e32 v7, 31, v4
	v_mad_u64_u32 v[4:5], s[10:11], v4, s12, 0
	v_mov_b32_e32 v6, v5
	v_ashrrev_i32_e32 v1, 6, v130
	v_mad_u64_u32 v[6:7], s[10:11], v7, s12, v[6:7]
	v_mov_b32_e32 v5, v6
	v_add_u32_e32 v6, s20, v1
	v_ashrrev_i32_e32 v9, 31, v6
	v_mad_u64_u32 v[6:7], s[10:11], v6, s12, 0
	v_mov_b32_e32 v8, v7
	v_mad_u64_u32 v[8:9], s[10:11], v9, s12, v[8:9]
	v_mov_b32_e32 v7, v8
	v_lshl_add_u64 v[4:5], v[4:5], 2, v[2:3]
	v_lshl_add_u64 v[2:3], v[6:7], 2, v[2:3]
	global_load_dwordx4 v[6:9], v[4:5], off
	s_nop 0
	global_load_dwordx4 v[2:5], v[2:3], off
	v_lshlrev_b32_e32 v45, 3, v130
	v_and_b32_e32 v66, 56, v45
	s_movk_i32 s0, 0x400
	v_mad_u32_u24 v55, v66, s0, 0
	v_mul_lo_u32 v57, v1, s0
	v_mul_lo_u32 v58, v38, s0
	v_mul_lo_u32 v59, v39, s0
	v_mul_lo_u32 v60, v40, s0
	v_mul_lo_u32 v61, v41, s0
	v_mul_lo_u32 v62, v42, s0
	v_mul_lo_u32 v63, v43, s0
	v_mul_lo_u32 v64, v44, s0
	s_add_u32 s0, s6, 0x1e940000
	s_addc_u32 s9, s7, 0
	s_add_u32 s12, s6, 0x16940000
	s_addc_u32 s13, s7, 0
	s_add_u32 s14, s78, 0x1000000
	s_addc_u32 s15, s79, 0
	s_add_u32 s16, s6, 0x16140000
	s_addc_u32 s17, s7, 0
	v_readlane_b32 s56, v250, 7
	s_add_u32 s36, s6, 0x15540000
	v_readlane_b32 s70, v250, 21
	v_readlane_b32 s71, v250, 22
	s_addc_u32 s37, s7, 0
	s_mov_b64 s[18:19], s[70:71]
	s_add_u32 s18, s18, 0x6c00000
	s_addc_u32 s19, s19, 0
	s_add_u32 s6, s6, 0x11f40000
	v_add_u32_e32 v34, 0, v34
	v_ashrrev_i32_e32 v45, 3, v130
	v_ashrrev_i32_e32 v48, 3, v37
	v_ashrrev_i32_e32 v51, 3, v51
	v_ashrrev_i32_e32 v54, 3, v54
	s_addc_u32 s7, s7, 0
	s_add_i32 s10, s33, s40
	s_mov_b32 s11, 0
	v_xor_b32_e32 v47, v45, v66
	v_lshl_add_u32 v46, v47, 2, v55
	v_and_b32_e32 v47, 15, v45
	v_xor_b32_e32 v50, v48, v66
	v_lshl_add_u32 v49, v50, 2, v55
	v_and_b32_e32 v50, 15, v48
	v_xor_b32_e32 v53, v51, v66
	v_lshl_add_u32 v52, v53, 2, v55
	v_and_b32_e32 v53, 15, v51
	v_xor_b32_e32 v56, v54, v66
	v_lshl_add_u32 v55, v56, 2, v55
	v_and_b32_e32 v56, 15, v54
	s_add_i32 s38, s10, 0xfffff5c0
	s_add_i32 s39, s10, 0xfffff6c0
	v_add_u32_e32 v57, v34, v57
	v_add_u32_e32 v58, v34, v58
	v_xor_b32_e32 v58, 32, v58
	v_add_u32_e32 v59, v34, v59
	v_xor_b32_e32 v59, 64, v59
	v_add_u32_e32 v60, v34, v60
	v_xor_b32_e32 v60, 96, v60
	v_add_u32_e32 v61, v34, v61
	v_xor_b32_e32 v61, 128, v61
	v_add_u32_e32 v62, v34, v62
	v_xor_b32_e32 v62, 160, v62
	v_add_u32_e32 v63, v34, v63
	v_xor_b32_e32 v63, 192, v63
	v_add_u32_e32 v64, v34, v64
	v_xor_b32_e32 v64, 224, v64
	v_lshlrev_b32_e32 v34, 2, v36
	v_lshlrev_b32_e32 v36, 1, v66
	s_movk_i32 s41, 0x7fff
	v_mov_b32_e32 v65, 1
	s_mov_b32 s10, s21
	s_mov_b32 s42, s35
	s_mov_b64 s[24:25], s[2:3]
	v_readlane_b32 s57, v250, 8
	v_readlane_b32 s58, v250, 9
	v_readlane_b32 s59, v250, 10
	v_readlane_b32 s60, v250, 11
	v_readlane_b32 s61, v250, 12
	v_readlane_b32 s62, v250, 13
	v_readlane_b32 s63, v250, 14
	v_readlane_b32 s64, v250, 15
	v_readlane_b32 s65, v250, 16
	v_readlane_b32 s66, v250, 17
	v_readlane_b32 s67, v250, 18
	v_readlane_b32 s68, v250, 19
	v_readlane_b32 s69, v250, 20
	s_waitcnt vmcnt(0)
	s_branch .LBB0_2317

.LBB0_2317:
	s_add_i32 s33, s33, s40
	s_cmp_lt_u32 s34, 2
	s_cselect_b64 s[22:23], -1, 0
	s_and_b64 vcc, exec, s[22:23]
	s_mov_b32 s43, s1
	s_mov_b32 s26, s8
	s_mov_b32 s30, s20
	s_waitcnt vmcnt(4)
	ds_write_b128 v57, v[2:5]
	ds_write_b128 v58, v[6:9]
	ds_write_b128 v59, v[10:13]
	ds_write_b128 v60, v[14:17]
	ds_write_b128 v61, v[18:21]
	ds_write_b128 v62, v[22:25]
	ds_write_b128 v63, v[26:29]
	ds_write_b128 v64, v[30:33]
	s_waitcnt lgkmcnt(0)
	s_barrier
	s_cbranch_vccnz .LBB0_2316
	s_add_i32 s30, s38, 0xa40
	s_cmpk_lt_i32 s30, 0x6c0
	s_cbranch_scc1 .LBB0_2314
	s_cmpk_gt_u32 s30, 0x83f
	s_mov_b64 s[26:27], -1
	s_cbranch_scc0 .LBB0_2332
	s_cmpk_gt_u32 s30, 0x93f
	s_cbranch_scc0 .LBB0_2329
	s_add_i32 s24, s38, 0x100
	s_mul_hi_u32 s10, s39, 0xaaaaaaab
	s_mul_hi_u32 s24, s24, 0xaaaaaaab
	s_lshr_b32 s10, s10, 8
	s_lshr_b32 s26, s24, 8
	s_mulk_i32 s10, 0xfe80
	s_mul_i32 s24, s26, 0xfffffe80
	s_add_i32 s46, s33, s24
	s_add_i32 s45, s38, s10
	s_addk_i32 s46, 0xf6c0
	s_add_i32 s27, s45, 0x100
	s_cmpk_gt_i32 s27, 0x7f
	s_mov_b64 s[30:31], -1
	s_cbranch_scc0 .LBB0_2326
	s_cmpk_gt_u32 s27, 0xff
	s_cbranch_scc0 .LBB0_2324
	s_add_i32 s10, s26, 16
	s_lshl_b64 s[24:25], s[10:11], 23
	s_mov_b32 s27, s11
	s_add_u32 s28, s88, s24
	s_addc_u32 s29, s89, s25
	s_lshl_b64 s[24:25], s[26:27], 22
	s_add_u32 s24, s0, s24
	s_addc_u32 s25, s9, s25
	s_mov_b64 s[30:31], 0

.LBB0_3747:
	s_waitcnt vmcnt(5)
	v_add_u32_e32 v2, 0x800, v34
	s_lshr_b32 s4, s8, 8
	v_ashrrev_i32_e32 v42, 6, v2
	v_cvt_f32_u32_e32 v2, s4
	s_sub_i32 s11, 0, s4
	s_abs_i32 s10, s9
	s_ashr_i32 s5, s9, 31
	v_rcp_iflag_f32_e32 v2, v2
	v_add_u32_e32 v3, 0xa00, v34
	v_ashrrev_i32_e32 v43, 6, v3
	v_add_u32_e32 v3, 0xc00, v34
	v_mul_f32_e32 v2, 0x4f7ffffe, v2
	v_cvt_u32_f32_e32 v2, v2
	v_lshlrev_b32_e32 v1, 2, v34
	v_ashrrev_i32_e32 v44, 6, v3
	v_add_u32_e32 v3, 0xe00, v34
	v_readfirstlane_b32 s12, v2
	s_mul_i32 s11, s11, s12
	s_mul_hi_u32 s11, s12, s11
	s_add_i32 s12, s12, s11
	s_mul_hi_u32 s11, s10, s12
	s_mul_i32 s12, s11, s4
	s_sub_i32 s10, s10, s12
	s_add_i32 s12, s11, 1
	s_sub_i32 s13, s10, s4
	s_cmp_ge_u32 s10, s4
	s_cselect_b32 s11, s12, s11
	s_cselect_b32 s10, s13, s10
	s_add_i32 s12, s11, 1
	s_cmp_ge_u32 s10, s4
	s_cselect_b32 s10, s12, s11
	s_xor_b32 s10, s10, s5
	s_sub_i32 s12, s10, s5
	s_mul_i32 s4, s12, s4
	s_sub_i32 s4, s9, s4
	s_lshl_b32 s4, s4, 8
	s_ashr_i32 s5, s4, 31
	s_lshl_b64 s[10:11], s[4:5], 2
	s_add_u32 s6, s6, s10
	v_and_b32_e32 v38, 0xfc, v1
	v_ashrrev_i32_e32 v45, 6, v3
	s_addc_u32 s7, s7, s11
	s_lshl_b32 s18, s12, 6
	v_mov_b32_e32 v37, 0
	v_lshlrev_b32_e32 v36, 2, v38
	v_add_u32_e32 v2, s18, v45
	v_lshl_add_u64 v[26:27], s[6:7], 0, v[36:37]
	v_ashrrev_i32_e32 v5, 31, v2
	v_mad_u64_u32 v[2:3], s[6:7], v2, s8, 0
	v_mov_b32_e32 v4, v3
	v_mad_u64_u32 v[4:5], s[6:7], v5, s8, v[4:5]
	v_mov_b32_e32 v3, v4
	v_lshl_add_u64 v[10:11], v[2:3], 2, v[26:27]
	v_add_u32_e32 v2, s18, v44
	v_ashrrev_i32_e32 v5, 31, v2
	v_mad_u64_u32 v[2:3], s[6:7], v2, s8, 0
	v_mov_b32_e32 v4, v3
	v_mad_u64_u32 v[4:5], s[6:7], v5, s8, v[4:5]
	v_mov_b32_e32 v3, v4
	v_lshl_add_u64 v[12:13], v[2:3], 2, v[26:27]
	global_load_dwordx4 v[6:9], v[10:11], off
	global_load_dwordx4 v[2:5], v[12:13], off
	v_add_u32_e32 v10, s18, v43
	v_ashrrev_i32_e32 v13, 31, v10
	v_mad_u64_u32 v[10:11], s[6:7], v10, s8, 0
	v_mov_b32_e32 v12, v11
	v_mad_u64_u32 v[12:13], s[6:7], v13, s8, v[12:13]
	v_mov_b32_e32 v11, v12
	v_lshl_add_u64 v[18:19], v[10:11], 2, v[26:27]
	v_add_u32_e32 v10, s18, v42
	v_ashrrev_i32_e32 v13, 31, v10
	v_mad_u64_u32 v[10:11], s[6:7], v10, s8, 0
	v_mov_b32_e32 v12, v11
	v_add_u32_e32 v55, 0x600, v34
	v_mad_u64_u32 v[12:13], s[6:7], v13, s8, v[12:13]
	v_ashrrev_i32_e32 v41, 6, v55
	v_mov_b32_e32 v11, v12
	v_lshl_add_u64 v[20:21], v[10:11], 2, v[26:27]
	global_load_dwordx4 v[14:17], v[18:19], off
	global_load_dwordx4 v[10:13], v[20:21], off
	v_add_u32_e32 v18, s18, v41
	v_ashrrev_i32_e32 v21, 31, v18
	v_mad_u64_u32 v[18:19], s[6:7], v18, s8, 0
	v_mov_b32_e32 v20, v19
	v_add_u32_e32 v52, 0x400, v34
	v_mad_u64_u32 v[20:21], s[6:7], v21, s8, v[20:21]
	v_ashrrev_i32_e32 v40, 6, v52
	v_mov_b32_e32 v19, v20
	v_lshl_add_u64 v[28:29], v[18:19], 2, v[26:27]
	v_add_u32_e32 v18, s18, v40
	v_ashrrev_i32_e32 v21, 31, v18
	v_mad_u64_u32 v[18:19], s[6:7], v18, s8, 0
	v_mov_b32_e32 v20, v19
	v_add_u32_e32 v39, 0x200, v34
	v_mad_u64_u32 v[20:21], s[6:7], v21, s8, v[20:21]
	v_ashrrev_i32_e32 v35, 6, v39
	v_mov_b32_e32 v19, v20
	s_waitcnt vmcnt(8)
	v_lshl_add_u64 v[30:31], v[18:19], 2, v[26:27]
	global_load_dwordx4 v[22:25], v[28:29], off
	global_load_dwordx4 v[18:21], v[30:31], off
	v_add_u32_e32 v28, s18, v35
	v_ashrrev_i32_e32 v31, 31, v28
	v_mad_u64_u32 v[28:29], s[6:7], v28, s8, 0
	v_mov_b32_e32 v30, v29
	v_mad_u64_u32 v[30:31], s[6:7], v31, s8, v[30:31]
	v_ashrrev_i32_e32 v1, 6, v34
	v_mov_b32_e32 v29, v30
	v_lshl_add_u64 v[46:47], v[28:29], 2, v[26:27]
	v_add_u32_e32 v28, s18, v1
	v_ashrrev_i32_e32 v31, 31, v28
	v_mad_u64_u32 v[28:29], s[6:7], v28, s8, 0
	v_mov_b32_e32 v30, v29
	v_mad_u64_u32 v[30:31], s[6:7], v31, s8, v[30:31]
	v_mov_b32_e32 v29, v30
	v_lshl_add_u64 v[48:49], v[28:29], 2, v[26:27]
	global_load_dwordx4 v[30:33], v[46:47], off
	global_load_dwordx4 v[26:29], v[48:49], off
	v_lshlrev_b32_e32 v46, 3, v34
	v_and_b32_e32 v66, 56, v46
	s_movk_i32 s5, 0x400
	v_readlane_b32 s16, v252, 3
	v_mad_u32_u24 v56, v66, s5, 0
	v_mul_lo_u32 v58, v1, s5
	v_mul_lo_u32 v59, v35, s5
	v_mul_lo_u32 v60, v40, s5
	v_mul_lo_u32 v61, v41, s5
	v_mul_lo_u32 v62, v42, s5
	v_mul_lo_u32 v63, v43, s5
	v_mul_lo_u32 v64, v44, s5
	v_mul_lo_u32 v65, v45, s5
	v_readlane_b32 s17, v252, 4
	s_add_u32 s5, s16, 0x1e940000
	s_addc_u32 s30, s17, 0
	s_add_u32 s8, s16, 0x16940000
	s_addc_u32 s9, s17, 0
	s_add_u32 s10, s78, 0x1000000
	s_addc_u32 s11, s79, 0
	s_add_u32 s12, s16, 0x16140000
	s_addc_u32 s13, s17, 0
	v_readlane_b32 s36, v250, 7
	s_add_u32 s31, s16, 0x15540000
	v_readlane_b32 s50, v250, 21
	v_readlane_b32 s51, v250, 22
	s_addc_u32 s33, s17, 0
	s_mov_b64 s[14:15], s[50:51]
	s_add_u32 s14, s14, 0x6c00000
	s_addc_u32 s15, s15, 0
	v_add_u32_e32 v36, 0, v36
	v_ashrrev_i32_e32 v46, 3, v34
	v_ashrrev_i32_e32 v49, 3, v39
	v_ashrrev_i32_e32 v52, 3, v52
	v_ashrrev_i32_e32 v55, 3, v55
	v_readlane_b32 s38, v250, 9
	s_add_u32 s16, s16, 0x11f40000
	s_mov_b32 s7, 0
	v_xor_b32_e32 v48, v46, v66
	v_lshl_add_u32 v47, v48, 2, v56
	v_and_b32_e32 v48, 15, v46
	v_xor_b32_e32 v51, v49, v66
	v_lshl_add_u32 v50, v51, 2, v56
	v_and_b32_e32 v51, 15, v49
	v_xor_b32_e32 v54, v52, v66
	v_lshl_add_u32 v53, v54, 2, v56
	v_and_b32_e32 v54, 15, v52
	v_xor_b32_e32 v57, v55, v66
	v_lshl_add_u32 v56, v57, 2, v56
	v_and_b32_e32 v57, 15, v55
	s_addc_u32 s17, s17, 0
	s_add_i32 s34, s20, 0x15e1
	s_mov_b32 s35, 17
	v_add_u32_e32 v58, v36, v58
	v_add_u32_e32 v59, v36, v59
	v_xor_b32_e32 v59, 32, v59
	v_add_u32_e32 v60, v36, v60
	v_xor_b32_e32 v60, 64, v60
	v_add_u32_e32 v61, v36, v61
	v_xor_b32_e32 v61, 96, v61
	v_add_u32_e32 v62, v36, v62
	v_xor_b32_e32 v62, 128, v62
	v_add_u32_e32 v63, v36, v63
	v_xor_b32_e32 v63, 160, v63
	v_add_u32_e32 v64, v36, v64
	v_xor_b32_e32 v64, 192, v64
	v_add_u32_e32 v65, v36, v65
	v_xor_b32_e32 v65, 224, v65
	v_lshlrev_b32_e32 v36, 2, v38
	v_lshlrev_b32_e32 v38, 1, v66
	s_movk_i32 s36, 0x7fff
	v_mov_b32_e32 v66, 1
	s_mov_b32 s6, s19
	s_mov_b32 s38, s0
	s_mov_b64 s[22:23], s[2:3]
	v_readlane_b32 s37, v250, 8
	v_readlane_b32 s39, v250, 10
	v_readlane_b32 s40, v250, 11
	v_readlane_b32 s41, v250, 12
	v_readlane_b32 s42, v250, 13
	v_readlane_b32 s43, v250, 14
	v_readlane_b32 s44, v250, 15
	v_readlane_b32 s45, v250, 16
	v_readlane_b32 s46, v250, 17
	v_readlane_b32 s47, v250, 18
	v_readlane_b32 s48, v250, 19
	v_readlane_b32 s49, v250, 20
	s_waitcnt vmcnt(0)
	s_branch .LBB0_3751

.LBB0_3751:
	s_add_i32 s37, s28, 1
	s_cmp_lt_u32 s35, 2
	s_cselect_b64 s[20:21], -1, 0
	s_and_b64 vcc, exec, s[20:21]
	s_mov_b32 s39, s1
	s_mov_b32 s24, s4
	s_mov_b32 s29, s18
	s_waitcnt vmcnt(4)
	ds_write_b128 v58, v[26:29]
	ds_write_b128 v59, v[30:33]
	ds_write_b128 v60, v[18:21]
	ds_write_b128 v61, v[22:25]
	ds_write_b128 v62, v[10:13]
	ds_write_b128 v63, v[14:17]
	ds_write_b128 v64, v[2:5]
	ds_write_b128 v65, v[6:9]
	s_waitcnt lgkmcnt(0)
	s_barrier
	s_cbranch_vccnz .LBB0_3750
	s_add_i32 s6, s34, 0x93f
	s_cmpk_lt_i32 s6, 0x6bf
	s_cbranch_scc1 .LBB0_3748
	s_add_i32 s29, s34, 0x940
	s_cmpk_gt_u32 s29, 0x83f
	s_mov_b64 s[24:25], -1
	s_cbranch_scc0 .LBB0_3766
	s_cmpk_gt_u32 s29, 0x93f
	s_cbranch_scc0 .LBB0_3763
	s_mul_hi_u32 s6, s34, 0xaaaaaaab
	s_lshr_b32 s24, s6, 8
	s_mul_i32 s6, s24, 0xfffffe80
	s_add_i32 s42, s28, s6
	s_addk_i32 s42, 0xf6c1
	s_add_i32 s25, s34, s6
	s_cmpk_gt_i32 s25, 0x7f
	s_mov_b64 s[28:29], -1
	s_cbranch_scc0 .LBB0_3760
	s_cmpk_gt_u32 s25, 0xff
	s_cbranch_scc0 .LBB0_3758
	s_add_i32 s6, s24, 16
	s_add_i32 s41, s42, 0xffffff00
	s_lshl_b64 s[22:23], s[6:7], 23
	s_mov_b32 s25, s7
	s_add_u32 s26, s88, s22
	s_addc_u32 s27, s89, s23
	s_lshl_b64 s[22:23], s[24:25], 22
	s_add_u32 s22, s5, s22
	s_addc_u32 s23, s30, s23
	s_mov_b64 s[28:29], 0

.LBB0_3796:
	s_waitcnt vmcnt(5)
	v_add_u32_e32 v2, 0x800, v34
	s_lshr_b32 s0, s8, 8
	v_ashrrev_i32_e32 v42, 6, v2
	v_cvt_f32_u32_e32 v2, s0
	s_sub_i32 s10, 0, s0
	s_abs_i32 s5, s9
	s_ashr_i32 s4, s9, 31
	v_rcp_iflag_f32_e32 v2, v2
	v_add_u32_e32 v3, 0xa00, v34
	v_ashrrev_i32_e32 v43, 6, v3
	v_add_u32_e32 v3, 0xc00, v34
	v_mul_f32_e32 v2, 0x4f7ffffe, v2
	v_cvt_u32_f32_e32 v2, v2
	v_lshlrev_b32_e32 v1, 2, v34
	v_ashrrev_i32_e32 v44, 6, v3
	v_add_u32_e32 v3, 0xe00, v34
	v_readfirstlane_b32 s11, v2
	s_mul_i32 s10, s10, s11
	s_mul_hi_u32 s10, s11, s10
	s_add_i32 s11, s11, s10
	s_mul_hi_u32 s10, s5, s11
	s_mul_i32 s11, s10, s0
	s_sub_i32 s5, s5, s11
	s_add_i32 s11, s10, 1
	s_sub_i32 s12, s5, s0
	s_cmp_ge_u32 s5, s0
	s_cselect_b32 s10, s11, s10
	s_cselect_b32 s5, s12, s5
	s_add_i32 s11, s10, 1
	s_cmp_ge_u32 s5, s0
	s_cselect_b32 s5, s11, s10
	s_xor_b32 s5, s5, s4
	s_sub_i32 s12, s5, s4
	s_mul_i32 s0, s12, s0
	s_sub_i32 s0, s9, s0
	s_lshl_b32 s4, s0, 8
	s_ashr_i32 s5, s4, 31
	s_lshl_b64 s[10:11], s[4:5], 2
	s_add_u32 s6, s6, s10
	v_and_b32_e32 v38, 0xfc, v1
	v_ashrrev_i32_e32 v45, 6, v3
	s_addc_u32 s7, s7, s11
	s_lshl_b32 s18, s12, 6
	v_mov_b32_e32 v37, 0
	v_lshlrev_b32_e32 v36, 2, v38
	v_add_u32_e32 v2, s18, v45
	v_lshl_add_u64 v[26:27], s[6:7], 0, v[36:37]
	v_ashrrev_i32_e32 v5, 31, v2
	v_mad_u64_u32 v[2:3], s[6:7], v2, s8, 0
	v_mov_b32_e32 v4, v3
	v_mad_u64_u32 v[4:5], s[6:7], v5, s8, v[4:5]
	v_mov_b32_e32 v3, v4
	v_lshl_add_u64 v[10:11], v[2:3], 2, v[26:27]
	v_add_u32_e32 v2, s18, v44
	v_ashrrev_i32_e32 v5, 31, v2
	v_mad_u64_u32 v[2:3], s[6:7], v2, s8, 0
	v_mov_b32_e32 v4, v3
	v_mad_u64_u32 v[4:5], s[6:7], v5, s8, v[4:5]
	v_mov_b32_e32 v3, v4
	v_lshl_add_u64 v[12:13], v[2:3], 2, v[26:27]
	global_load_dwordx4 v[6:9], v[10:11], off
	global_load_dwordx4 v[2:5], v[12:13], off
	v_add_u32_e32 v10, s18, v43
	v_ashrrev_i32_e32 v13, 31, v10
	v_mad_u64_u32 v[10:11], s[6:7], v10, s8, 0
	v_mov_b32_e32 v12, v11
	v_mad_u64_u32 v[12:13], s[6:7], v13, s8, v[12:13]
	v_mov_b32_e32 v11, v12
	v_lshl_add_u64 v[18:19], v[10:11], 2, v[26:27]
	v_add_u32_e32 v10, s18, v42
	v_ashrrev_i32_e32 v13, 31, v10
	v_mad_u64_u32 v[10:11], s[6:7], v10, s8, 0
	v_mov_b32_e32 v12, v11
	v_add_u32_e32 v55, 0x600, v34
	v_mad_u64_u32 v[12:13], s[6:7], v13, s8, v[12:13]
	v_ashrrev_i32_e32 v41, 6, v55
	v_mov_b32_e32 v11, v12
	v_lshl_add_u64 v[20:21], v[10:11], 2, v[26:27]
	global_load_dwordx4 v[14:17], v[18:19], off
	global_load_dwordx4 v[10:13], v[20:21], off
	v_add_u32_e32 v18, s18, v41
	v_ashrrev_i32_e32 v21, 31, v18
	v_mad_u64_u32 v[18:19], s[6:7], v18, s8, 0
	v_mov_b32_e32 v20, v19
	v_add_u32_e32 v52, 0x400, v34
	v_mad_u64_u32 v[20:21], s[6:7], v21, s8, v[20:21]
	v_ashrrev_i32_e32 v40, 6, v52
	v_mov_b32_e32 v19, v20
	v_lshl_add_u64 v[28:29], v[18:19], 2, v[26:27]
	v_add_u32_e32 v18, s18, v40
	v_ashrrev_i32_e32 v21, 31, v18
	v_mad_u64_u32 v[18:19], s[6:7], v18, s8, 0
	v_mov_b32_e32 v20, v19
	v_add_u32_e32 v35, 0x200, v34
	v_mad_u64_u32 v[20:21], s[6:7], v21, s8, v[20:21]
	v_ashrrev_i32_e32 v39, 6, v35
	v_mov_b32_e32 v19, v20
	s_waitcnt vmcnt(8)
	v_lshl_add_u64 v[30:31], v[18:19], 2, v[26:27]
	global_load_dwordx4 v[22:25], v[28:29], off
	global_load_dwordx4 v[18:21], v[30:31], off
	v_add_u32_e32 v28, s18, v39
	v_ashrrev_i32_e32 v31, 31, v28
	v_mad_u64_u32 v[28:29], s[6:7], v28, s8, 0
	v_mov_b32_e32 v30, v29
	v_mad_u64_u32 v[30:31], s[6:7], v31, s8, v[30:31]
	v_ashrrev_i32_e32 v1, 6, v34
	v_mov_b32_e32 v29, v30
	v_lshl_add_u64 v[46:47], v[28:29], 2, v[26:27]
	v_add_u32_e32 v28, s18, v1
	v_ashrrev_i32_e32 v31, 31, v28
	v_mad_u64_u32 v[28:29], s[6:7], v28, s8, 0
	v_mov_b32_e32 v30, v29
	v_mad_u64_u32 v[30:31], s[6:7], v31, s8, v[30:31]
	v_mov_b32_e32 v29, v30
	v_lshl_add_u64 v[48:49], v[28:29], 2, v[26:27]
	global_load_dwordx4 v[30:33], v[46:47], off
	global_load_dwordx4 v[26:29], v[48:49], off
	v_lshlrev_b32_e32 v46, 3, v34
	v_and_b32_e32 v66, 56, v46
	s_movk_i32 s0, 0x400
	v_readlane_b32 s16, v252, 3
	v_mad_u32_u24 v56, v66, s0, 0
	v_mul_lo_u32 v58, v1, s0
	v_mul_lo_u32 v59, v39, s0
	v_mul_lo_u32 v60, v40, s0
	v_mul_lo_u32 v61, v41, s0
	v_mul_lo_u32 v62, v42, s0
	v_mul_lo_u32 v63, v43, s0
	v_mul_lo_u32 v64, v44, s0
	v_mul_lo_u32 v65, v45, s0
	v_readlane_b32 s17, v252, 4
	s_add_u32 s0, s16, 0x1e940000
	s_addc_u32 s5, s17, 0
	s_add_u32 s8, s16, 0x16940000
	s_addc_u32 s9, s17, 0
	s_add_u32 s10, s78, 0x1000000
	s_addc_u32 s11, s79, 0
	s_add_u32 s12, s16, 0x16140000
	s_addc_u32 s13, s17, 0
	v_readlane_b32 s36, v250, 7
	s_add_u32 s31, s16, 0x15540000
	v_readlane_b32 s50, v250, 21
	v_readlane_b32 s51, v250, 22
	s_addc_u32 s33, s17, 0
	s_mov_b64 s[14:15], s[50:51]
	s_add_u32 s14, s14, 0x6c00000
	s_addc_u32 s15, s15, 0
	v_add_u32_e32 v36, 0, v36
	v_ashrrev_i32_e32 v46, 3, v34
	v_ashrrev_i32_e32 v49, 3, v35
	v_ashrrev_i32_e32 v52, 3, v52
	v_ashrrev_i32_e32 v55, 3, v55
	v_readlane_b32 s38, v250, 9
	s_add_u32 s16, s16, 0x11f40000
	s_mov_b32 s7, 0
	v_xor_b32_e32 v48, v46, v66
	v_lshl_add_u32 v47, v48, 2, v56
	v_and_b32_e32 v48, 15, v46
	v_xor_b32_e32 v51, v49, v66
	v_lshl_add_u32 v50, v51, 2, v56
	v_and_b32_e32 v51, 15, v49
	v_xor_b32_e32 v54, v52, v66
	v_lshl_add_u32 v53, v54, 2, v56
	v_and_b32_e32 v54, 15, v52
	v_xor_b32_e32 v57, v55, v66
	v_lshl_add_u32 v56, v57, 2, v56
	v_and_b32_e32 v57, 15, v55
	s_addc_u32 s17, s17, 0
	s_add_i32 s34, s20, 0xfffffce1
	s_mov_b32 s35, 25
	v_add_u32_e32 v58, v36, v58
	v_add_u32_e32 v59, v36, v59
	v_xor_b32_e32 v59, 32, v59
	v_add_u32_e32 v60, v36, v60
	v_xor_b32_e32 v60, 64, v60
	v_add_u32_e32 v61, v36, v61
	v_xor_b32_e32 v61, 96, v61
	v_add_u32_e32 v62, v36, v62
	v_xor_b32_e32 v62, 128, v62
	v_add_u32_e32 v63, v36, v63
	v_xor_b32_e32 v63, 160, v63
	v_add_u32_e32 v64, v36, v64
	v_xor_b32_e32 v64, 192, v64
	v_add_u32_e32 v65, v36, v65
	v_xor_b32_e32 v65, 224, v65
	v_lshlrev_b32_e32 v36, 2, v38
	v_lshlrev_b32_e32 v34, 1, v66
	s_movk_i32 s36, 0x7fff
	v_mov_b32_e32 v38, 1
	s_mov_b32 s6, s19
	s_mov_b32 s38, s30
	s_mov_b64 s[22:23], s[2:3]
	v_readlane_b32 s37, v250, 8
	v_readlane_b32 s39, v250, 10
	v_readlane_b32 s40, v250, 11
	v_readlane_b32 s41, v250, 12
	v_readlane_b32 s42, v250, 13
	v_readlane_b32 s43, v250, 14
	v_readlane_b32 s44, v250, 15
	v_readlane_b32 s45, v250, 16
	v_readlane_b32 s46, v250, 17
	v_readlane_b32 s47, v250, 18
	v_readlane_b32 s48, v250, 19
	v_readlane_b32 s49, v250, 20
	s_waitcnt vmcnt(0)
	s_branch .LBB0_3800

.LBB0_3800:
	s_add_i32 s37, s28, 1
	s_cmp_lt_u32 s35, 2
	s_cselect_b64 s[20:21], -1, 0
	s_and_b64 vcc, exec, s[20:21]
	s_mov_b32 s39, s1
	s_mov_b32 s24, s4
	s_mov_b32 s29, s18
	s_waitcnt vmcnt(4)
	ds_write_b128 v58, v[26:29]
	ds_write_b128 v59, v[30:33]
	ds_write_b128 v60, v[18:21]
	ds_write_b128 v61, v[22:25]
	ds_write_b128 v62, v[10:13]
	ds_write_b128 v63, v[14:17]
	ds_write_b128 v64, v[2:5]
	ds_write_b128 v65, v[6:9]
	s_waitcnt lgkmcnt(0)
	s_barrier
	s_cbranch_vccnz .LBB0_3799
	s_add_i32 s6, s34, 0x93f
	s_cmpk_lt_i32 s6, 0x6bf
	s_cbranch_scc1 .LBB0_3797
	s_add_i32 s29, s34, 0x940
	s_cmpk_gt_u32 s29, 0x83f
	s_mov_b64 s[24:25], -1
	s_cbranch_scc0 .LBB0_3815
	s_cmpk_gt_u32 s29, 0x93f
	s_cbranch_scc0 .LBB0_3812
	s_mul_hi_u32 s6, s34, 0xaaaaaaab
	s_lshr_b32 s24, s6, 8
	s_mul_i32 s6, s24, 0xfffffe80
	s_add_i32 s42, s28, s6
	s_addk_i32 s42, 0xf6c1
	s_add_i32 s25, s34, s6
	s_cmpk_gt_i32 s25, 0x7f
	s_mov_b64 s[28:29], -1
	s_cbranch_scc0 .LBB0_3809
	s_cmpk_gt_u32 s25, 0xff
	s_cbranch_scc0 .LBB0_3807
	s_add_i32 s6, s24, 16
	s_add_i32 s41, s42, 0xffffff00
	s_lshl_b64 s[22:23], s[6:7], 23
	s_mov_b32 s25, s7
	s_add_u32 s26, s88, s22
	s_addc_u32 s27, s89, s23
	s_lshl_b64 s[22:23], s[24:25], 22
	s_add_u32 s22, s0, s22
	s_addc_u32 s23, s5, s23
	s_mov_b64 s[28:29], 0
